# attention steps: K LDS reads issued before the step's two LDS-DMA requests
# speedup vs baseline: 1.0134x; 1.0074x over previous
; #define ATT_DMA(t, slot) do { glds16(ksrc + (long)(t) * tstep, (unsigned)__builtin_amdgcn_readfirstlane(kdst + (slot))); glds16(vsrc + (long)(t) * tstep, (unsigned)__builtin_amdgcn_readfirstlane(vdst + (slot))); } while (0)
;     __device__ __forceinline__ void init(f32x16& c0, f32x16& c1, int t) const {
;         float base = slope2 * ((float)(64 * t + 4 * hi) - tqf);
;         if (t < nb0) { if (!((selmask >> (t >> 2)) & 1u)) base = ATT_NEG; }
;         const float d32 = 32.0f * slope2;
; #pragma unroll
;         for (int i = 0; i < 8; ++i) { const int r = 2 * i; const f32x2_t kc = (f32x2_t){slope2 * (float)((r & 3) + 8 * (r >> 2)), slope2 * (float)(((r + 1) & 3) + 8 * ((r + 1) >> 2))};
;             const f32x2_t p = kc + base, q = p + d32; c0[r] = p[0]; c0[r + 1] = p[1]; c1[r] = q[0]; c1[r + 1] = q[1]; }
;         if (t - nb0 == (w >> 1)) {
; #pragma unroll
;             for (int r = 0; r < 16; ++r) { const int ko = (r & 3) + 8 * (r >> 2); if (ko > u) c0[r] = ATT_NEG; if (ko > u - 32) c1[r] = ATT_NEG; }
;         }
;     }
; template <class BIAS>
; __device__ __forceinline__ void attn_tiles(char* shm, const UnitIO& io, int t_begin, int t_end, const BIAS& B, int tid) {
;     ...
;         if (rem > 3) ATT_DMA(t + 3, ((t + 3 - t_begin) & 3) * SLOTB);
;         u32x4 pw[4]; f32x16 c1x;
;         if (act) {
;             bf16x8 kf[8]; const lds_cptr kp = kp0 + sl_c;
; #pragma unroll
;             for (int j = 0; j < 4; ++j) { kf[2 * j] = *(const __attribute__((address_space(3))) bf16x8*)(kp + j * 2048); kf[2 * j + 1] = *(const __attribute__((address_space(3))) bf16x8*)(kp + j * 2048 + 512); }
.LBB0_298:
	s_add_i32 s34, s20, s17
	s_cmp_lt_u32 s17, s26
	s_cselect_b64 s[14:15], -1, 0
	s_cmp_le_i32 s34, s73
	s_cselect_b64 s[4:5], -1, 0
	s_or_b64 vcc, s[14:15], s[4:5]
	s_add_i32 s4, s22, 0xffffa000
	v_cndmask_b32_e64 v58, 0, 1, vcc
	s_and_b32 s23, s4, 0x6000
	v_cmp_ne_u32_e64 s[4:5], 1, v58
	s_andn2_b64 vcc, exec, vcc
	s_cbranch_vccnz .Lmo_inact
	v_add_u32_e32 v34, s23, v181
	ds_read_b128 v[98:101], v34
	ds_read_b128 v[94:97], v34 offset:512
	ds_read_b128 v[102:105], v34 offset:2048
	ds_read_b128 v[90:93], v34 offset:2560
	ds_read_b128 v[106:109], v34 offset:4096
	ds_read_b128 v[86:89], v34 offset:4608
	ds_read_b128 v[110:113], v34 offset:6144
	ds_read_b128 v[82:85], v34 offset:6656
	s_and_b64 vcc, exec, s[12:13]
	s_cbranch_vccnz .Lmo_nodmaA
	s_and_b32 s100, s22, 0x6000
	s_add_i32 s101, s100, s29
	s_mov_b32 m0, s101
	s_add_i32 s100, s100, s33
	global_load_lds_dwordx4 v[172:173], off
	s_mov_b32 m0, s100
	s_nop 0
	global_load_lds_dwordx4 v[152:153], off
.Lmo_nodmaA:
	s_add_i32 s35, s24, s17
	v_cvt_f32_u32_e32 v34, v149
	s_lshr_b32 vcc_lo, s17, 2
	s_lshl_b32 vcc_lo, 1, vcc_lo
	v_and_b32_e32 v35, vcc_lo, v135
	v_sub_f32_e32 v34, v34, v137
	v_cmp_eq_u32_e32 vcc, 0, v35
	v_mul_f32_e32 v34, v115, v34
	s_and_b64 vcc, s[14:15], vcc
	v_cndmask_b32_e32 v34, v34, v226, vcc
	v_add_f32_e32 v50, v114, v34
	v_add_f32_e32 v51, v115, v34
	v_add_f32_e32 v52, v118, v34
	v_add_f32_e32 v53, v119, v34
	v_add_f32_e32 v54, v120, v34
	v_add_f32_e32 v55, v121, v34
	v_add_f32_e32 v56, v122, v34
	v_add_f32_e32 v57, v123, v34
	v_add_f32_e32 v58, v124, v34
	v_add_f32_e32 v59, v125, v34
	v_add_f32_e32 v60, v126, v34
	v_add_f32_e32 v61, v127, v34
	v_add_f32_e32 v62, v128, v34
	v_add_f32_e32 v63, v129, v34
	v_add_f32_e32 v64, v140, v34
	v_add_f32_e32 v65, v141, v34
	v_mov_b32_e32 v117, v116
	v_add_f32_e32 v48, v116, v64
	v_add_f32_e32 v49, v117, v65
	v_add_f32_e32 v46, v116, v62
	v_add_f32_e32 v47, v117, v63
	v_add_f32_e32 v44, v116, v60
	v_add_f32_e32 v45, v117, v61
	v_add_f32_e32 v42, v116, v58
	v_add_f32_e32 v43, v117, v59
	v_add_f32_e32 v40, v116, v56
	v_add_f32_e32 v41, v117, v57
	v_add_f32_e32 v38, v116, v54
	v_add_f32_e32 v39, v117, v55
	v_add_f32_e32 v36, v116, v52
	v_add_f32_e32 v37, v117, v53
	s_cmp_lg_u32 s35, 0
	v_add_f32_e32 v34, v162, v50
	v_add_f32_e32 v35, v163, v51
	s_cbranch_scc1 .LBB0_303
	v_cndmask_b32_e64 v48, v48, v226, s[36:37]
	v_cndmask_b32_e64 v47, v47, v226, s[40:41]
	v_cndmask_b32_e64 v46, v46, v226, s[42:43]
	v_cndmask_b32_e64 v45, v45, v226, s[44:45]
	v_cndmask_b32_e64 v44, v44, v226, s[46:47]
	v_cndmask_b32_e64 v43, v43, v226, s[48:49]
	v_cndmask_b32_e64 v42, v42, v226, s[50:51]
	v_cndmask_b32_e64 v41, v41, v226, s[52:53]
	v_cndmask_b32_e64 v40, v40, v226, s[54:55]
	v_cndmask_b32_e64 v39, v39, v226, s[56:57]
	v_cndmask_b32_e64 v38, v38, v226, s[58:59]
	v_cndmask_b32_e64 v37, v37, v226, s[60:61]
	v_cndmask_b32_e64 v36, v36, v226, s[62:63]
	v_cndmask_b32_e64 v35, v35, v226, s[64:65]
	v_cndmask_b32_e64 v34, v34, v226, s[66:67]
	s_and_saveexec_b64 s[14:15], s[6:7]
	s_mov_b32 s35, 0xff800000
	v_mov_b32_e32 v49, s35
	s_or_b64 exec, exec, s[14:15]
	v_cndmask_b32_e64 v65, v65, v226, s[38:39]
	v_cndmask_b32_e64 v50, v50, v226, s[96:97]
	v_cndmask_b32_e64 v51, v51, v226, s[94:95]
	v_cndmask_b32_e64 v52, v52, v226, s[92:93]
	v_cndmask_b32_e64 v53, v53, v226, s[90:91]
	v_cndmask_b32_e64 v54, v54, v226, s[88:89]
	v_cndmask_b32_e64 v55, v55, v226, s[2:3]
	v_cndmask_b32_e64 v56, v56, v226, s[84:85]
	v_cndmask_b32_e64 v57, v57, v226, s[82:83]
	v_cndmask_b32_e64 v58, v58, v226, s[80:81]
	v_cndmask_b32_e64 v59, v59, v226, s[78:79]
	v_cndmask_b32_e64 v60, v60, v226, s[76:77]
	v_cndmask_b32_e64 v61, v61, v226, s[74:75]
	v_cndmask_b32_e64 v62, v62, v226, s[18:19]
	v_cndmask_b32_e64 v63, v63, v226, s[70:71]
	v_cndmask_b32_e64 v64, v64, v226, s[68:69]

; #define ATT_DMA(t, slot) do { glds16(ksrc + (long)(t) * tstep, (unsigned)__builtin_amdgcn_readfirstlane(kdst + (slot))); glds16(vsrc + (long)(t) * tstep, (unsigned)__builtin_amdgcn_readfirstlane(vdst + (slot))); } while (0)
; template <class BIAS>
; __device__ __forceinline__ void attn_tiles(char* shm, const UnitIO& io, int t_begin, int t_end, const BIAS& B, int tid) {
;     ...
;         if (rem > 3) ATT_DMA(t + 3, ((t + 3 - t_begin) & 3) * SLOTB);
.Lmo_inact:
	s_and_b64 vcc, exec, s[12:13]
	s_cbranch_vccnz .Lmo_nodmaB
	s_and_b32 s100, s22, 0x6000
	s_add_i32 s101, s100, s29
	s_mov_b32 m0, s101
	s_add_i32 s100, s100, s33
	global_load_lds_dwordx4 v[172:173], off
	s_mov_b32 m0, s100
	s_nop 0
	global_load_lds_dwordx4 v[152:153], off
.Lmo_nodmaB:
.LBB0_310:
	s_and_b64 vcc, exec, s[4:5]
	s_cbranch_vccnz .LBB0_304

; #define ATT_SBAR() __builtin_amdgcn_sched_barrier(0)
; #define ATT_DMA(t, slot) do { glds16(ksrc + (long)(t) * tstep, (unsigned)__builtin_amdgcn_readfirstlane(kdst + (slot))); glds16(vsrc + (long)(t) * tstep, (unsigned)__builtin_amdgcn_readfirstlane(vdst + (slot))); } while (0)
;     __device__ __forceinline__ void init(f32x16& c0, f32x16& c1, int t) const {
;         const lds_fptr p = cs2 + 64 * t + 4 * hi;
;         f32x4 a[4], b[4];
; #pragma unroll
;         for (int g = 0; g < 4; ++g) { a[g] = *(const __attribute__((address_space(3))) f32x4*)(p + 8 * g); b[g] = *(const __attribute__((address_space(3))) f32x4*)(p + 32 + 8 * g); }
;         asm volatile("" : "+v"(a[0]), "+v"(a[1]), "+v"(a[2]), "+v"(a[3]), "+v"(b[0]), "+v"(b[1]), "+v"(b[2]), "+v"(b[3]));
; #pragma unroll
;         for (int g = 0; g < 4; ++g) { const f32x2_t a0 = (f32x2_t){a[g][0], a[g][1]}, a1 = (f32x2_t){a[g][2], a[g][3]}, b0 = (f32x2_t){b[g][0], b[g][1]}, b1 = (f32x2_t){b[g][2], b[g][3]};
;             const f32x2_t x0 = base - a0, x1 = base - a1, y0 = base - b0, y1 = base - b1;
;             c0[4 * g] = x0[0]; c0[4 * g + 1] = x0[1]; c0[4 * g + 2] = x1[0]; c0[4 * g + 3] = x1[1]; c1[4 * g] = y0[0]; c1[4 * g + 1] = y0[1]; c1[4 * g + 2] = y1[0]; c1[4 * g + 3] = y1[1]; }
;         if (t - nb0 == (w >> 1)) {
; #pragma unroll
;             for (int r = 0; r < 16; ++r) { const int ko = (r & 3) + 8 * (r >> 2); if (ko > u) c0[r] = ATT_NEG; if (ko > u - 32) c1[r] = ATT_NEG; }
;         }
; template <class BIAS>
; __device__ __forceinline__ void attn_tiles(char* shm, const UnitIO& io, int t_begin, int t_end, const BIAS& B, int tid) {
;     ...
;         if (rem > 3) ATT_DMA(t + 3, ((t + 3 - t_begin) & 3) * SLOTB);
;         u32x4 pw[4]; f32x16 c1x;
;         if (act) {
;             bf16x8 kf[8]; const lds_cptr kp = kp0 + sl_c;
; #pragma unroll
;             for (int j = 0; j < 4; ++j) { kf[2 * j] = *(const __attribute__((address_space(3))) bf16x8*)(kp + j * 2048); kf[2 * j + 1] = *(const __attribute__((address_space(3))) bf16x8*)(kp + j * 2048 + 512); }
;             ATT_SBAR();
;             f32x16 c0, c1; B.init(c0, c1, t);
.LBB0_341:
.LBB0_342:
	s_add_i32 s20, s44, -3
	s_add_i32 s45, s37, s44
	s_cmp_lt_i32 s20, s51
	s_cselect_b64 s[20:21], -1, 0
	s_add_i32 s22, s45, -3
	s_cmp_le_i32 s22, s73
	s_cselect_b64 s[34:35], -1, 0
	s_or_b64 vcc, s[20:21], s[34:35]
	s_add_i32 s20, s39, 0xffffa000
	v_cndmask_b32_e64 v74, 0, 1, vcc
	s_and_b32 s20, s20, 0x6000
	v_cmp_ne_u32_e64 s[34:35], 1, v74
	s_andn2_b64 vcc, exec, vcc
	s_cbranch_vccnz .Lfx_inact
	v_add_u32_e32 v50, s20, v181
	ds_read_b128 v[114:117], v50
	ds_read_b128 v[110:113], v50 offset:512
	ds_read_b128 v[118:121], v50 offset:2048
	ds_read_b128 v[106:109], v50 offset:2560
	ds_read_b128 v[122:125], v50 offset:4096
	ds_read_b128 v[102:105], v50 offset:4608
	ds_read_b128 v[126:129], v50 offset:6144
	ds_read_b128 v[98:101], v50 offset:6656
	s_add_i32 s21, s36, s44
	ds_read_b128 v[50:53], v137 offset:224
	ds_read_b128 v[54:57], v137 offset:192
	ds_read_b128 v[58:61], v137 offset:96
	ds_read_b128 v[62:65], v137 offset:64
	ds_read_b128 v[218:221], v137 offset:160
	ds_read_b128 v[234:237], v137 offset:128
	ds_read_b128 v[66:69], v137
	ds_read_b128 v[70:73], v137 offset:32
	s_and_b64 vcc, exec, s[46:47]
	s_cbranch_vccnz .Lfx_nodmaA
	s_mov_b32 s100, s44
	s_ashr_i32 s101, s44, 31
	s_lshl_b64 s[100:101], s[100:101], 17
	s_add_u32 s100, s100, 0x200
	s_addc_u32 s101, s101, 0
	v_lshl_add_u64 v[74:75], v[144:145], 0, s[100:101]
	s_and_b32 s22, s39, 0x6000
	s_add_i32 s23, s22, s27
	s_mov_b32 m0, s23
	s_add_i32 s22, s22, s33
	global_load_lds_dwordx4 v[74:75], off
	v_lshl_add_u64 v[74:75], v[154:155], 0, s[100:101]
	s_mov_b32 m0, s22
	s_nop 0
	global_load_lds_dwordx4 v[74:75], off
.Lfx_nodmaA:
	s_cmp_lg_u32 s21, 3
	s_waitcnt lgkmcnt(0)
	s_nop 0
	v_sub_f32_e32 v81, v33, v61
	v_sub_f32_e32 v80, v32, v60
	v_sub_f32_e32 v79, v31, v59
	v_sub_f32_e32 v78, v30, v58
	v_sub_f32_e32 v77, v29, v65
	v_sub_f32_e32 v76, v28, v64
	v_sub_f32_e32 v75, v11, v63
	v_sub_f32_e32 v74, v10, v62
	v_sub_f32_e32 v73, v9, v73
	v_sub_f32_e32 v72, v8, v72
	v_sub_f32_e32 v71, v7, v71
	v_sub_f32_e32 v70, v6, v70
	v_sub_f32_e32 v69, v5, v69
	v_sub_f32_e32 v68, v4, v68
	v_sub_f32_e32 v67, v3, v67
	v_sub_f32_e32 v66, v2, v66
	v_sub_f32_e32 v65, v33, v53
	v_sub_f32_e32 v64, v32, v52
	v_sub_f32_e32 v63, v31, v51
	v_sub_f32_e32 v62, v30, v50
	v_sub_f32_e32 v61, v29, v57
	v_sub_f32_e32 v60, v28, v56
	v_sub_f32_e32 v59, v11, v55
	v_sub_f32_e32 v58, v10, v54
	v_sub_f32_e32 v57, v9, v221
	v_sub_f32_e32 v56, v8, v220
	v_sub_f32_e32 v55, v7, v219
	v_sub_f32_e32 v54, v6, v218
	v_sub_f32_e32 v53, v5, v237
	v_sub_f32_e32 v52, v4, v236
	v_sub_f32_e32 v51, v3, v235
	v_sub_f32_e32 v50, v2, v234
	s_cbranch_scc1 .LBB0_347
	v_cndmask_b32_e64 v64, v64, v226, s[56:57]
	v_cndmask_b32_e64 v63, v63, v226, s[60:61]
	v_cndmask_b32_e64 v62, v62, v226, s[62:63]
	v_cndmask_b32_e64 v61, v61, v226, s[64:65]
	v_cndmask_b32_e64 v60, v60, v226, s[66:67]
	v_cndmask_b32_e64 v59, v59, v226, s[0:1]
	v_cndmask_b32_e64 v58, v58, v226, s[40:41]
	v_cndmask_b32_e64 v57, v57, v226, s[68:69]
	v_cndmask_b32_e64 v56, v56, v226, s[70:71]
	v_cndmask_b32_e64 v55, v55, v226, s[48:49]
	v_cndmask_b32_e64 v54, v54, v226, s[74:75]
	v_cndmask_b32_e64 v53, v53, v226, s[76:77]
	v_cndmask_b32_e64 v52, v52, v226, s[78:79]
	v_cndmask_b32_e64 v51, v51, v226, s[80:81]
	v_cndmask_b32_e64 v50, v50, v226, s[82:83]
	s_and_saveexec_b64 vcc, s[30:31]
	s_mov_b32 s21, 0xff800000
	v_mov_b32_e32 v65, s21
	s_or_b64 exec, exec, vcc
	v_cndmask_b32_e64 v81, v81, v226, s[58:59]
	v_cndmask_b32_e64 v80, v80, v226, s[84:85]
	v_cndmask_b32_e64 v79, v79, v226, s[2:3]
	v_cndmask_b32_e64 v78, v78, v226, s[88:89]
	v_cndmask_b32_e64 v77, v77, v226, s[90:91]
	v_cndmask_b32_e64 v76, v76, v226, s[92:93]
	v_cndmask_b32_e64 v75, v75, v226, s[94:95]
	v_cndmask_b32_e64 v74, v74, v226, s[96:97]
	v_cndmask_b32_e64 v73, v73, v226, s[4:5]
	v_cndmask_b32_e64 v72, v72, v226, s[6:7]
	v_cndmask_b32_e64 v71, v71, v226, s[8:9]
	v_cndmask_b32_e64 v70, v70, v226, s[10:11]
	v_cndmask_b32_e64 v69, v69, v226, s[12:13]
	v_cndmask_b32_e64 v68, v68, v226, s[14:15]
	v_cndmask_b32_e64 v67, v67, v226, s[16:17]
	v_cndmask_b32_e64 v66, v66, v226, s[18:19]

; #define ATT_DMA(t, slot) do { glds16(ksrc + (long)(t) * tstep, (unsigned)__builtin_amdgcn_readfirstlane(kdst + (slot))); glds16(vsrc + (long)(t) * tstep, (unsigned)__builtin_amdgcn_readfirstlane(vdst + (slot))); } while (0)
; template <class BIAS>
; __device__ __forceinline__ void attn_tiles(char* shm, const UnitIO& io, int t_begin, int t_end, const BIAS& B, int tid) {
;     ...
;         if (rem > 3) ATT_DMA(t + 3, ((t + 3 - t_begin) & 3) * SLOTB);
.LBB0_353:
	s_cbranch_execz .LBB0_357
	s_branch .LBB0_358
	s_branch .LBB0_354
.Lfx_inact:
	s_and_b64 vcc, exec, s[46:47]
	s_cbranch_vccnz .Lfx_nodmaB
	s_mov_b32 s100, s44
	s_ashr_i32 s101, s44, 31
	s_lshl_b64 s[100:101], s[100:101], 17
	s_add_u32 s100, s100, 0x200
	s_addc_u32 s101, s101, 0
	v_lshl_add_u64 v[74:75], v[144:145], 0, s[100:101]
	s_and_b32 s22, s39, 0x6000
	s_add_i32 s23, s22, s27
	s_mov_b32 m0, s23
	s_add_i32 s22, s22, s33
	global_load_lds_dwordx4 v[74:75], off
	v_lshl_add_u64 v[74:75], v[154:155], 0, s[100:101]
	s_mov_b32 m0, s22
	s_nop 0
	global_load_lds_dwordx4 v[74:75], off
.Lfx_nodmaB:
.LBB0_354:
	s_and_b64 vcc, exec, s[34:35]
	s_cbranch_vccnz .LBB0_348

; #define ATT_SBAR() __builtin_amdgcn_sched_barrier(0)
; #define ATT_DMA(t, slot) do { glds16(ksrc + (long)(t) * tstep, (unsigned)__builtin_amdgcn_readfirstlane(kdst + (slot))); glds16(vsrc + (long)(t) * tstep, (unsigned)__builtin_amdgcn_readfirstlane(vdst + (slot))); } while (0)
;     __device__ __forceinline__ void init(f32x16& c0, f32x16& c1, int t) const {
;         const int dt = t - (w >> 1);
;         const float base = basel + (float)dt * d64;
; #pragma unroll
;         for (int i = 0; i < 8; ++i) { const f32x2_t p = kc[i] + base, q = p + d32; c0[2 * i] = p[0]; c0[2 * i + 1] = p[1]; c1[2 * i] = q[0]; c1[2 * i + 1] = q[1]; }
;         if (dt == 0) {
; #pragma unroll
;             for (int r = 0; r < 16; ++r) { const int ko = (r & 3) + 8 * (r >> 2); if (ko < u) c0[r] = ATT_NEG; if (ko < u - 32) c1[r] = ATT_NEG; }
;         } else if (dt == 2) {
; #pragma unroll
;             for (int r = 0; r < 16; ++r) { const int ko = (r & 3) + 8 * (r >> 2); if (ko > u) c0[r] = ATT_NEG; if (ko > u - 32) c1[r] = ATT_NEG; }
;         }
;     }
; template <class BIAS>
; __device__ __forceinline__ void attn_tiles(char* shm, const UnitIO& io, int t_begin, int t_end, const BIAS& B, int tid) {
;     ...
;         if (rem > 3) ATT_DMA(t + 3, ((t + 3 - t_begin) & 3) * SLOTB);
;         u32x4 pw[4]; f32x16 c1x;
;         if (act) {
;             bf16x8 kf[8]; const lds_cptr kp = kp0 + sl_c;
; #pragma unroll
;             for (int j = 0; j < 4; ++j) { kf[2 * j] = *(const __attribute__((address_space(3))) bf16x8*)(kp + j * 2048); kf[2 * j + 1] = *(const __attribute__((address_space(3))) bf16x8*)(kp + j * 2048 + 512); }
;             ATT_SBAR();
;             f32x16 c0, c1; B.init(c0, c1, t);
.LBB0_367:
	s_cmp_ge_i32 s88, s73
	s_cselect_b64 s[56:57], -1, 0
	s_cmp_le_i32 s88, s33
	s_cselect_b64 s[70:71], -1, 0
	s_and_b64 s[70:71], s[56:57], s[70:71]
	s_add_i32 s56, s81, 0xffffa000
	v_cndmask_b32_e64 v58, 0, 1, s[70:71]
	s_and_b32 s82, s56, 0x6000
	v_cmp_ne_u32_e64 s[56:57], 1, v58
	s_andn2_b64 vcc, exec, s[70:71]
	s_cbranch_vccnz .Ldl_inact
	v_add_u32_e32 v34, s82, v181
	ds_read_b128 v[130:133], v34
	ds_read_b128 v[126:129], v34 offset:512
	ds_read_b128 v[134:137], v34 offset:2048
	ds_read_b128 v[122:125], v34 offset:2560
	ds_read_b128 v[138:141], v34 offset:4096
	ds_read_b128 v[118:121], v34 offset:4608
	ds_read_b128 v[142:145], v34 offset:6144
	ds_read_b128 v[114:117], v34 offset:6656
	s_and_b64 vcc, exec, s[68:69]
	s_cbranch_vccnz .Ldl_nodmaA
	s_add_u32 s100, s88, 3
	s_addc_u32 s101, s89, 0
	s_lshl_b64 s[100:101], s[100:101], s80
	s_lshl_b64 s[100:101], s[100:101], 1
	s_add_u32 s100, s100, 0x500
	s_addc_u32 s101, s101, 0
	v_lshl_add_u64 v[58:59], v[172:173], 0, s[100:101]
	s_and_b32 s70, s81, 0x6000
	s_add_i32 s71, s70, s78
	s_mov_b32 m0, s71
	s_add_i32 s70, s70, s79
	global_load_lds_dwordx4 v[58:59], off
	v_lshl_add_u64 v[58:59], v[174:175], 0, s[100:101]
	s_mov_b32 m0, s70
	s_nop 0
	global_load_lds_dwordx4 v[58:59], off
.Ldl_nodmaA:
	s_add_u32 s70, s72, s88
	v_cvt_f32_i32_e32 v34, s70
	v_mov_b32_e32 v157, v156
	v_fma_f32 v34, v149, v34, -v0
	v_add_f32_e32 v82, v154, v34
	v_add_f32_e32 v83, v155, v34
	v_add_f32_e32 v84, v158, v34
	v_add_f32_e32 v85, v159, v34
	v_add_f32_e32 v86, v160, v34
	v_add_f32_e32 v87, v161, v34
	v_add_f32_e32 v88, v162, v34
	v_add_f32_e32 v89, v163, v34
	v_add_f32_e32 v90, v164, v34
	v_add_f32_e32 v91, v165, v34
	v_add_f32_e32 v92, v166, v34
	v_add_f32_e32 v93, v167, v34
	v_add_f32_e32 v94, v168, v34
	v_add_f32_e32 v95, v169, v34
	v_add_f32_e32 v96, v170, v34
	v_add_f32_e32 v97, v171, v34
	v_add_f32_e32 v46, v156, v94
	v_add_f32_e32 v47, v157, v95
	v_add_f32_e32 v48, v156, v96
	v_add_f32_e32 v49, v157, v97
	v_add_f32_e32 v44, v156, v92
	v_add_f32_e32 v45, v157, v93
	v_add_f32_e32 v42, v156, v90
	v_add_f32_e32 v43, v157, v91
	v_add_f32_e32 v40, v156, v88
	v_add_f32_e32 v41, v157, v89
	v_add_f32_e32 v38, v156, v86
	v_add_f32_e32 v39, v157, v87
	v_add_f32_e32 v36, v156, v84
	v_add_f32_e32 v37, v157, v85
	v_add_f32_e32 v34, v176, v82
	v_add_f32_e32 v35, v177, v83
	s_cmp_eq_u32 s70, 1
	s_cbranch_scc1 .Ldil_h1_go
	s_cmp_eq_u32 s70, 0
	s_cbranch_scc0 .Ldil_m2
	v_cndmask_b32_e64 v82, v82, v226, s[6:7]
	v_cndmask_b32_e64 v83, v83, v226, s[10:11]
	v_cndmask_b32_e64 v84, v84, v226, s[14:15]
	v_cndmask_b32_e64 v85, v85, v226, s[18:19]
	v_cndmask_b32_e64 v86, v86, v226, s[22:23]
	v_cndmask_b32_e64 v87, v87, v226, s[26:27]
	v_cndmask_b32_e64 v88, v88, v226, s[92:93]
	v_cndmask_b32_e64 v89, v89, v226, s[96:97]
	v_cndmask_b32_e64 v90, v90, v226, s[4:5]
	v_cndmask_b32_e64 v91, v91, v226, s[60:61]
	v_cndmask_b32_e64 v92, v92, v226, s[30:31]
	v_cndmask_b32_e64 v93, v93, v226, s[58:59]
	v_cndmask_b32_e64 v94, v94, v226, s[40:41]
	v_cndmask_b32_e64 v95, v95, v226, s[44:45]
	v_cndmask_b32_e64 v96, v96, v226, s[48:49]
	v_cndmask_b32_e64 v34, v34, v226, s[8:9]
	v_cndmask_b32_e64 v35, v35, v226, s[12:13]
	v_cndmask_b32_e64 v36, v36, v226, s[16:17]
	v_cndmask_b32_e64 v37, v37, v226, s[20:21]
	v_cndmask_b32_e64 v38, v38, v226, s[24:25]
	v_cndmask_b32_e64 v39, v39, v226, s[90:91]
	v_cndmask_b32_e64 v40, v40, v226, s[94:95]
	v_cndmask_b32_e64 v41, v41, v226, s[34:35]
	v_cndmask_b32_e64 v42, v42, v226, s[0:1]
	v_cndmask_b32_e64 v43, v43, v226, s[28:29]
	v_cndmask_b32_e64 v44, v44, v226, s[36:37]
	v_cndmask_b32_e64 v45, v45, v226, s[38:39]
	v_cndmask_b32_e64 v46, v46, v226, s[42:43]
	v_cndmask_b32_e64 v47, v47, v226, s[46:47]
	v_cndmask_b32_e64 v48, v48, v226, s[50:51]
	v_cndmask_b32_e64 v97, v97, v226, s[52:53]
	v_cndmask_b32_e64 v49, v49, v226, s[54:55]
	s_branch .Ldil_h1_go

; #define ATT_DMA(t, slot) do { glds16(ksrc + (long)(t) * tstep, (unsigned)__builtin_amdgcn_readfirstlane(kdst + (slot))); glds16(vsrc + (long)(t) * tstep, (unsigned)__builtin_amdgcn_readfirstlane(vdst + (slot))); } while (0)
; template <class BIAS>
; __device__ __forceinline__ void attn_tiles(char* shm, const UnitIO& io, int t_begin, int t_end, const BIAS& B, int tid) {
;     ...
;         if (rem > 3) ATT_DMA(t + 3, ((t + 3 - t_begin) & 3) * SLOTB);
.Ldl_inact:
	s_and_b64 vcc, exec, s[68:69]
	s_cbranch_vccnz .Ldl_nodmaB
	s_add_u32 s100, s88, 3
	s_addc_u32 s101, s89, 0
	s_lshl_b64 s[100:101], s[100:101], s80
	s_lshl_b64 s[100:101], s[100:101], 1
	s_add_u32 s100, s100, 0x500
	s_addc_u32 s101, s101, 0
	v_lshl_add_u64 v[58:59], v[172:173], 0, s[100:101]
	s_and_b32 s70, s81, 0x6000
	s_add_i32 s71, s70, s78
	s_mov_b32 m0, s71
	s_add_i32 s70, s70, s79
	global_load_lds_dwordx4 v[58:59], off
	v_lshl_add_u64 v[58:59], v[174:175], 0, s[100:101]
	s_mov_b32 m0, s70
	s_nop 0
	global_load_lds_dwordx4 v[58:59], off
.Ldl_nodmaB:
.LBB0_374:
	s_and_b64 vcc, exec, s[56:57]
	s_cbranch_vccnz .LBB0_381
